# MoE down epilogue (first-rank path): eight routing weights loaded together with the slot->token entries, no per-row-group vmcnt(0) behind the stores
# baseline (speedup 1.0000x reference)
.LBB0_1451:
	s_lshl_b32 s86, s85, 8
	s_add_i32 s86, s86, s94
	v_or_b32_e32 v192, s86, v49
	v_ashrrev_i32_e32 v193, 31, v192
	v_lshl_add_u64 v[130:131], v[192:193], 2, s[64:65]
	global_load_dword v194, v[130:131], off
	global_load_dword v190, v[130:131], off offset:64
	global_load_dword v188, v[130:131], off offset:128
	global_load_dword v186, v[130:131], off offset:192
	global_load_dword v176, v[130:131], off offset:512
	global_load_dword v174, v[130:131], off offset:576
	global_load_dword v172, v[130:131], off offset:640
	global_load_dword v168, v[130:131], off offset:704
	v_lshl_add_u64 v[228:229], v[192:193], 2, s[66:67]
	global_load_dword v220, v[228:229], off
	global_load_dword v221, v[228:229], off offset:64
	global_load_dword v222, v[228:229], off offset:128
	global_load_dword v223, v[228:229], off offset:192
	global_load_dword v224, v[228:229], off offset:512
	global_load_dword v225, v[228:229], off offset:576
	global_load_dword v226, v[228:229], off offset:640
	global_load_dword v227, v[228:229], off offset:704
	s_lshl_b32 s6, s83, 8
	s_or_b32 s83, s6, s95
	v_or_b32_e32 v138, 16, v192
	v_or_b32_e32 v140, 32, v192
	v_or_b32_e32 v142, 48, v192
	v_add_u32_e32 v178, 0x80, v192
	v_add_u32_e32 v180, 0x90, v192
	v_add_u32_e32 v182, 0xa0, v192
	v_add_u32_e32 v184, 0xb0, v192
	v_or_b32_e32 v170, s83, v201
	v_ashrrev_i32_e32 v139, 31, v138
	v_ashrrev_i32_e32 v141, 31, v140
	v_ashrrev_i32_e32 v143, 31, v142
	v_ashrrev_i32_e32 v179, 31, v178
	v_ashrrev_i32_e32 v181, 31, v180
	v_ashrrev_i32_e32 v183, 31, v182
	v_ashrrev_i32_e32 v185, 31, v184
	s_cmp_lt_i32 s85, s60
	v_ashrrev_i32_e32 v171, 31, v170
	s_waitcnt vmcnt(0)
	v_cmp_lt_i32_e32 vcc, -1, v194
	s_cbranch_scc1 .LBB0_1464
	s_and_saveexec_b64 s[6:7], vcc
	s_cbranch_execz .LBB0_1486
	v_mov_b32_e32 v134, v220
	v_mov_b32_e32 v195, v48
	v_lshlrev_b64 v[130:131], 11, v[194:195]
	v_lshl_add_u64 v[130:131], s[58:59], 0, v[130:131]
	v_lshl_add_u64 v[136:137], v[170:171], 1, v[130:131]
	v_pk_mul_f32 v[132:133], v[124:125], v[134:135] op_sel_hi:[1,0]
	v_pk_mul_f32 v[130:131], v[122:123], v[134:135] op_sel_hi:[1,0]
	v_pk_mul_f32 v[144:145], v[128:129], v[134:135] op_sel_hi:[1,0]
	v_pk_mul_f32 v[146:147], v[126:127], v[134:135] op_sel_hi:[1,0]
	v_cvt_pk_bf16_f32 v130, v130, v131
	v_cvt_pk_bf16_f32 v131, v132, v133
	v_cvt_pk_bf16_f32 v132, v146, v147
	v_cvt_pk_bf16_f32 v133, v144, v145
	global_store_dwordx4 v[136:137], v[130:133], off
	v_pk_mul_f32 v[144:145], v[116:117], v[134:135] op_sel_hi:[1,0]
	s_nop 0
	v_pk_mul_f32 v[132:133], v[120:121], v[134:135] op_sel_hi:[1,0]
	v_pk_mul_f32 v[130:131], v[118:119], v[134:135] op_sel_hi:[1,0]
	v_pk_mul_f32 v[134:135], v[114:115], v[134:135] op_sel_hi:[1,0]
	v_cvt_pk_bf16_f32 v130, v130, v131
	v_cvt_pk_bf16_f32 v131, v132, v133
	v_cvt_pk_bf16_f32 v132, v134, v135
	v_cvt_pk_bf16_f32 v133, v144, v145
	global_store_dwordx4 v[136:137], v[130:133], off offset:256
	s_or_b64 exec, exec, s[6:7]
	v_cmp_lt_i32_e32 vcc, -1, v190
	s_and_saveexec_b64 s[6:7], vcc
	s_cbranch_execnz .LBB0_1487

.LBB0_1455:
	v_mov_b32_e32 v134, v222
	v_mov_b32_e32 v189, v48
	v_lshlrev_b64 v[130:131], 11, v[188:189]
	v_lshl_add_u64 v[130:131], s[58:59], 0, v[130:131]
	v_lshl_add_u64 v[136:137], v[170:171], 1, v[130:131]
	v_pk_mul_f32 v[132:133], v[96:97], v[134:135] op_sel_hi:[1,0]
	v_pk_mul_f32 v[130:131], v[94:95], v[134:135] op_sel_hi:[1,0]
	v_pk_mul_f32 v[144:145], v[92:93], v[134:135] op_sel_hi:[1,0]
	v_pk_mul_f32 v[146:147], v[90:91], v[134:135] op_sel_hi:[1,0]
	v_cvt_pk_bf16_f32 v130, v130, v131
	v_cvt_pk_bf16_f32 v131, v132, v133
	v_cvt_pk_bf16_f32 v132, v146, v147
	v_cvt_pk_bf16_f32 v133, v144, v145
	global_store_dwordx4 v[136:137], v[130:133], off
	v_pk_mul_f32 v[144:145], v[84:85], v[134:135] op_sel_hi:[1,0]
	s_nop 0
	v_pk_mul_f32 v[132:133], v[88:89], v[134:135] op_sel_hi:[1,0]
	v_pk_mul_f32 v[130:131], v[86:87], v[134:135] op_sel_hi:[1,0]
	v_pk_mul_f32 v[134:135], v[82:83], v[134:135] op_sel_hi:[1,0]
	v_cvt_pk_bf16_f32 v130, v130, v131
	v_cvt_pk_bf16_f32 v131, v132, v133
	v_cvt_pk_bf16_f32 v132, v134, v135
	v_cvt_pk_bf16_f32 v133, v144, v145
	global_store_dwordx4 v[136:137], v[130:133], off offset:256
	s_or_b64 exec, exec, s[6:7]
	v_cmp_lt_i32_e32 vcc, -1, v186
	s_and_saveexec_b64 s[6:7], vcc
	s_cbranch_execnz .LBB0_1489

.LBB0_1457:
	v_mov_b32_e32 v134, v224
	v_mov_b32_e32 v177, v48
	v_lshlrev_b64 v[130:131], 11, v[176:177]
	v_lshl_add_u64 v[130:131], s[58:59], 0, v[130:131]
	v_lshl_add_u64 v[136:137], v[170:171], 1, v[130:131]
	v_pk_mul_f32 v[132:133], v[64:65], v[134:135] op_sel_hi:[1,0]
	v_pk_mul_f32 v[130:131], v[62:63], v[134:135] op_sel_hi:[1,0]
	v_pk_mul_f32 v[144:145], v[60:61], v[134:135] op_sel_hi:[1,0]
	v_pk_mul_f32 v[146:147], v[58:59], v[134:135] op_sel_hi:[1,0]
	v_cvt_pk_bf16_f32 v130, v130, v131
	v_cvt_pk_bf16_f32 v131, v132, v133
	v_cvt_pk_bf16_f32 v132, v146, v147
	v_cvt_pk_bf16_f32 v133, v144, v145
	global_store_dwordx4 v[136:137], v[130:133], off
	v_pk_mul_f32 v[144:145], v[52:53], v[134:135] op_sel_hi:[1,0]
	s_nop 0
	v_pk_mul_f32 v[132:133], v[56:57], v[134:135] op_sel_hi:[1,0]
	v_pk_mul_f32 v[130:131], v[54:55], v[134:135] op_sel_hi:[1,0]
	v_pk_mul_f32 v[134:135], v[50:51], v[134:135] op_sel_hi:[1,0]
	v_cvt_pk_bf16_f32 v130, v130, v131
	v_cvt_pk_bf16_f32 v131, v132, v133
	v_cvt_pk_bf16_f32 v132, v134, v135
	v_cvt_pk_bf16_f32 v133, v144, v145
	global_store_dwordx4 v[136:137], v[130:133], off offset:256
	s_or_b64 exec, exec, s[6:7]
	v_cmp_lt_i32_e32 vcc, -1, v174
	s_and_saveexec_b64 s[6:7], vcc
	s_cbranch_execnz .LBB0_1491

.LBB0_1459:
	v_mov_b32_e32 v134, v226
	v_mov_b32_e32 v173, v48
	v_lshlrev_b64 v[130:131], 11, v[172:173]
	v_lshl_add_u64 v[130:131], s[58:59], 0, v[130:131]
	v_lshl_add_u64 v[136:137], v[170:171], 1, v[130:131]
	v_pk_mul_f32 v[132:133], v[30:31], v[134:135] op_sel_hi:[1,0]
	v_pk_mul_f32 v[130:131], v[28:29], v[134:135] op_sel_hi:[1,0]
	v_pk_mul_f32 v[144:145], v[26:27], v[134:135] op_sel_hi:[1,0]
	v_pk_mul_f32 v[146:147], v[24:25], v[134:135] op_sel_hi:[1,0]
	v_cvt_pk_bf16_f32 v130, v130, v131
	v_cvt_pk_bf16_f32 v131, v132, v133
	v_cvt_pk_bf16_f32 v132, v146, v147
	v_cvt_pk_bf16_f32 v133, v144, v145
	global_store_dwordx4 v[136:137], v[130:133], off
	v_pk_mul_f32 v[144:145], v[18:19], v[134:135] op_sel_hi:[1,0]
	s_nop 0
	v_pk_mul_f32 v[132:133], v[22:23], v[134:135] op_sel_hi:[1,0]
	v_pk_mul_f32 v[130:131], v[20:21], v[134:135] op_sel_hi:[1,0]
	v_pk_mul_f32 v[134:135], v[16:17], v[134:135] op_sel_hi:[1,0]
	v_cvt_pk_bf16_f32 v130, v130, v131
	v_cvt_pk_bf16_f32 v131, v132, v133
	v_cvt_pk_bf16_f32 v132, v134, v135
	v_cvt_pk_bf16_f32 v133, v144, v145
	global_store_dwordx4 v[136:137], v[130:133], off offset:256
.LBB0_1460:
	s_or_b64 exec, exec, s[6:7]
	v_cmp_lt_i32_e32 vcc, -1, v168
	s_mov_b64 s[8:9], 0
	s_mov_b64 s[6:7], 0
	s_and_saveexec_b64 s[78:79], vcc
	s_xor_b64 s[78:79], exec, s[78:79]
	s_cbranch_execz .LBB0_1462
	v_mov_b32_e32 v134, v227
	v_mov_b32_e32 v169, v48
	v_lshlrev_b64 v[130:131], 11, v[168:169]
	v_lshl_add_u64 v[130:131], s[58:59], 0, v[130:131]
	v_lshl_add_u64 v[144:145], v[170:171], 1, v[130:131]
	s_mov_b64 s[6:7], exec
	v_pk_mul_f32 v[132:133], v[14:15], v[134:135] op_sel_hi:[1,0]
	v_pk_mul_f32 v[130:131], v[12:13], v[134:135] op_sel_hi:[1,0]
	v_pk_mul_f32 v[136:137], v[10:11], v[134:135] op_sel_hi:[1,0]
	v_pk_mul_f32 v[146:147], v[8:9], v[134:135] op_sel_hi:[1,0]
	v_cvt_pk_bf16_f32 v130, v130, v131
	v_cvt_pk_bf16_f32 v131, v132, v133
	v_cvt_pk_bf16_f32 v132, v146, v147
	v_cvt_pk_bf16_f32 v133, v136, v137
	global_store_dwordx4 v[144:145], v[130:133], off
	v_pk_mul_f32 v[136:137], v[2:3], v[134:135] op_sel_hi:[1,0]
	s_nop 0
	v_pk_mul_f32 v[132:133], v[6:7], v[134:135] op_sel_hi:[1,0]
	v_pk_mul_f32 v[130:131], v[4:5], v[134:135] op_sel_hi:[1,0]
	v_pk_mul_f32 v[134:135], v[0:1], v[134:135] op_sel_hi:[1,0]

.LBB0_1487:
	v_mov_b32_e32 v134, v221
	v_mov_b32_e32 v191, v48
	v_lshlrev_b64 v[130:131], 11, v[190:191]
	v_lshl_add_u64 v[130:131], s[58:59], 0, v[130:131]
	v_lshl_add_u64 v[136:137], v[170:171], 1, v[130:131]
	v_pk_mul_f32 v[132:133], v[112:113], v[134:135] op_sel_hi:[1,0]
	v_pk_mul_f32 v[130:131], v[110:111], v[134:135] op_sel_hi:[1,0]
	v_pk_mul_f32 v[144:145], v[108:109], v[134:135] op_sel_hi:[1,0]
	v_pk_mul_f32 v[146:147], v[106:107], v[134:135] op_sel_hi:[1,0]
	v_cvt_pk_bf16_f32 v130, v130, v131
	v_cvt_pk_bf16_f32 v131, v132, v133
	v_cvt_pk_bf16_f32 v132, v146, v147
	v_cvt_pk_bf16_f32 v133, v144, v145
	global_store_dwordx4 v[136:137], v[130:133], off
	v_pk_mul_f32 v[144:145], v[100:101], v[134:135] op_sel_hi:[1,0]
	s_nop 0
	v_pk_mul_f32 v[132:133], v[104:105], v[134:135] op_sel_hi:[1,0]
	v_pk_mul_f32 v[130:131], v[102:103], v[134:135] op_sel_hi:[1,0]
	v_pk_mul_f32 v[134:135], v[98:99], v[134:135] op_sel_hi:[1,0]
	v_cvt_pk_bf16_f32 v130, v130, v131
	v_cvt_pk_bf16_f32 v131, v132, v133
	v_cvt_pk_bf16_f32 v132, v134, v135
	v_cvt_pk_bf16_f32 v133, v144, v145
	global_store_dwordx4 v[136:137], v[130:133], off offset:256
	s_or_b64 exec, exec, s[6:7]
	v_cmp_lt_i32_e32 vcc, -1, v188
	s_and_saveexec_b64 s[6:7], vcc
	s_cbranch_execnz .LBB0_1455

.LBB0_1489:
	v_mov_b32_e32 v134, v223
	v_mov_b32_e32 v187, v48
	v_lshlrev_b64 v[130:131], 11, v[186:187]
	v_lshl_add_u64 v[130:131], s[58:59], 0, v[130:131]
	v_lshl_add_u64 v[136:137], v[170:171], 1, v[130:131]
	v_pk_mul_f32 v[132:133], v[80:81], v[134:135] op_sel_hi:[1,0]
	v_pk_mul_f32 v[130:131], v[78:79], v[134:135] op_sel_hi:[1,0]
	v_pk_mul_f32 v[144:145], v[76:77], v[134:135] op_sel_hi:[1,0]
	v_pk_mul_f32 v[146:147], v[74:75], v[134:135] op_sel_hi:[1,0]
	v_cvt_pk_bf16_f32 v130, v130, v131
	v_cvt_pk_bf16_f32 v131, v132, v133
	v_cvt_pk_bf16_f32 v132, v146, v147
	v_cvt_pk_bf16_f32 v133, v144, v145
	global_store_dwordx4 v[136:137], v[130:133], off
	v_pk_mul_f32 v[144:145], v[68:69], v[134:135] op_sel_hi:[1,0]
	s_nop 0
	v_pk_mul_f32 v[132:133], v[72:73], v[134:135] op_sel_hi:[1,0]
	v_pk_mul_f32 v[130:131], v[70:71], v[134:135] op_sel_hi:[1,0]
	v_pk_mul_f32 v[134:135], v[66:67], v[134:135] op_sel_hi:[1,0]
	v_cvt_pk_bf16_f32 v130, v130, v131
	v_cvt_pk_bf16_f32 v131, v132, v133
	v_cvt_pk_bf16_f32 v132, v134, v135
	v_cvt_pk_bf16_f32 v133, v144, v145
	global_store_dwordx4 v[136:137], v[130:133], off offset:256
	s_or_b64 exec, exec, s[6:7]
	v_cmp_lt_i32_e32 vcc, -1, v176
	s_and_saveexec_b64 s[6:7], vcc
	s_cbranch_execnz .LBB0_1457

.LBB0_1491:
	v_mov_b32_e32 v134, v225
	v_mov_b32_e32 v175, v48
	v_lshlrev_b64 v[130:131], 11, v[174:175]
	v_lshl_add_u64 v[130:131], s[58:59], 0, v[130:131]
	v_lshl_add_u64 v[136:137], v[170:171], 1, v[130:131]
	v_pk_mul_f32 v[132:133], v[46:47], v[134:135] op_sel_hi:[1,0]
	v_pk_mul_f32 v[130:131], v[44:45], v[134:135] op_sel_hi:[1,0]
	v_pk_mul_f32 v[144:145], v[42:43], v[134:135] op_sel_hi:[1,0]
	v_pk_mul_f32 v[146:147], v[40:41], v[134:135] op_sel_hi:[1,0]
	v_cvt_pk_bf16_f32 v130, v130, v131
	v_cvt_pk_bf16_f32 v131, v132, v133
	v_cvt_pk_bf16_f32 v132, v146, v147
	v_cvt_pk_bf16_f32 v133, v144, v145
	global_store_dwordx4 v[136:137], v[130:133], off
	v_pk_mul_f32 v[144:145], v[34:35], v[134:135] op_sel_hi:[1,0]
	s_nop 0
	v_pk_mul_f32 v[132:133], v[38:39], v[134:135] op_sel_hi:[1,0]
	v_pk_mul_f32 v[130:131], v[36:37], v[134:135] op_sel_hi:[1,0]
	v_pk_mul_f32 v[134:135], v[32:33], v[134:135] op_sel_hi:[1,0]
	v_cvt_pk_bf16_f32 v130, v130, v131
	v_cvt_pk_bf16_f32 v131, v132, v133
	v_cvt_pk_bf16_f32 v132, v134, v135
	v_cvt_pk_bf16_f32 v133, v144, v145
	global_store_dwordx4 v[136:137], v[130:133], off offset:256
	s_or_b64 exec, exec, s[6:7]
	v_cmp_lt_i32_e32 vcc, -1, v172
	s_and_saveexec_b64 s[6:7], vcc
	s_cbranch_execnz .LBB0_1459
	s_branch .LBB0_1460
